# previous best + scalar select/address group and s_setprio hoisted above the pre-MFMA barrier in the gate/up and down K-loops (SALU-only groups, pure move)
# baseline (speedup 1.0000x reference)
; #define G8_STAGE(bufoff, gbase, voff) do { _Pragma("unroll") for (int _i = 0; _i < 2; ++_i) \
;         __builtin_amdgcn_global_load_lds((const unsigned*)((const char*)(gbase) + (voff)[_i]), (LAS unsigned*)(lds + (bufoff) + ldsw + _i * 8192), 16, 0, 0); } while (0)
; #define G8_LDA(dst, b, h) do { _Pragma("unroll") for (int m = 0; m < 4; ++m) _Pragma("unroll") for (int k = 0; k < 2; ++k) dst[m][k] = *(const LAS bf16x8*)(lds + G8_SA(b, h) + aoff + m * 2048 + k * 1024); } while (0)
; #define G8_LDB(dst, b, h) do { _Pragma("unroll") for (int n = 0; n < 2; ++n) _Pragma("unroll") for (int k = 0; k < 2; ++k) dst[n][k] = *(const LAS bf16x8*)(lds + G8_SB(b, h) + boff + n * 2048 + k * 1024); } while (0)
; #define G8_MMA(ai, bj, At, Bt) do { __builtin_amdgcn_s_setprio(1); _Pragma("unroll") for (int m = 0; m < 4; ++m) _Pragma("unroll") for (int n = 0; n < 2; ++n) _Pragma("unroll") for (int k = 0; k < 2; ++k) \
;         acc[ai][bj][m][n] = __builtin_amdgcn_mfma_f32_16x16x32_bf16(Bt[n][k], At[m][k], acc[ai][bj][m][n], 0, 0, 0); __builtin_amdgcn_s_setprio(0); } while (0)
; #define G8_WAIT_V(n) asm volatile("s_waitcnt vmcnt(" #n ")" ::: "memory")
; #define G8_WAIT_L(n) asm volatile("s_waitcnt lgkmcnt(" #n ")" ::: "memory")
; #define G8_BAR __builtin_amdgcn_s_barrier()
; #define G8_SCHED __builtin_amdgcn_sched_barrier(0)
; template <class Epi, class Sched>
; __device__ __forceinline__ void gemm_phase(LAS unsigned char* lds, const int K, const Sched& S, const Epi& E) {
;     ...
;             const char* a1 = cA + (size_t)(t + 1) * kstep;
;             const char* a2 = last ? nA : cA + (size_t)(t + 2) * kstep; const char* b2 = last ? nB : cB + (size_t)(t + 2) * kstep;
;             const char* a3 = a2 + kstep; const char* b3 = b2 + kstep;
;             G8_LDB(B0, 0, 0); G8_SCHED; G8_LDA(At, 0, 0); G8_STAGE(G8_SA(1, 1), a1, oc[1]);
;             if (last && has_next) S.aoff(nxt, tid, oc);
;             G8_WAIT_L(8); G8_BAR; G8_WAIT_L(0); G8_MMA(0, 0, At, B0); G8_BAR; G8_SCHED;
;             G8_LDB(B1, 0, 1); G8_STAGE(G8_SB(0, 0), b2, voffB);
;             G8_BAR; G8_WAIT_L(0); G8_MMA(0, 1, At, B1); G8_BAR;
;             G8_LDA(At, 0, 1); G8_STAGE(G8_SA(0, 0), a2, oc[0]);
;             G8_BAR; G8_WAIT_L(0); G8_MMA(1, 0, At, B0); G8_BAR; G8_SCHED;
;             G8_STAGE(G8_SB(0, 1), b2 + hstep, voffB);
;             G8_WAIT_V(6); G8_BAR; G8_MMA(1, 1, At, B1); G8_BAR;
.LBB0_2526:
	s_add_u32 s34, s22, 0x80
	s_addc_u32 s35, s23, 0
	s_and_b64 s[24:25], s[24:25], exec
	s_cselect_b32 s35, s1, s35
	s_cselect_b32 s34, s0, s34
	s_cselect_b32 s25, s13, s56
	s_cselect_b32 s24, s12, s55
	s_setprio 1
	s_waitcnt lgkmcnt(8)
	s_barrier
	s_waitcnt lgkmcnt(0)
	s_waitcnt lgkmcnt(0)
	v_mfma_f32_16x16x32_bf16 v[126:129], v[130:133], v[170:173], v[126:129]
	v_mfma_f32_16x16x32_bf16 v[122:125], v[138:141], v[170:173], v[122:125]
	v_mfma_f32_16x16x32_bf16 v[110:113], v[130:133], v[162:165], v[110:113]
	v_mfma_f32_16x16x32_bf16 v[106:109], v[138:141], v[162:165], v[106:109]
	v_mfma_f32_16x16x32_bf16 v[94:97], v[130:133], v[154:157], v[94:97]
	v_mfma_f32_16x16x32_bf16 v[90:93], v[138:141], v[154:157], v[90:93]
	v_mfma_f32_16x16x32_bf16 v[78:81], v[130:133], v[146:149], v[78:81]
	v_mfma_f32_16x16x32_bf16 v[74:77], v[138:141], v[146:149], v[74:77]
	v_mfma_f32_16x16x32_bf16 v[126:129], v[134:137], v[174:177], v[126:129]
	v_mfma_f32_16x16x32_bf16 v[122:125], v[142:145], v[174:177], v[122:125]
	v_mfma_f32_16x16x32_bf16 v[110:113], v[134:137], v[166:169], v[110:113]
	v_mfma_f32_16x16x32_bf16 v[106:109], v[142:145], v[166:169], v[106:109]
	v_mfma_f32_16x16x32_bf16 v[94:97], v[134:137], v[158:161], v[94:97]
	v_mfma_f32_16x16x32_bf16 v[90:93], v[142:145], v[158:161], v[90:93]
	v_mfma_f32_16x16x32_bf16 v[78:81], v[134:137], v[150:153], v[78:81]
	v_mfma_f32_16x16x32_bf16 v[74:77], v[142:145], v[150:153], v[74:77]
	s_setprio 0
	s_barrier
	s_add_i32 s60, 0, 0x14000
	s_mov_b32 m0, s43
	v_add_u32_e32 v183, s60, v198
	v_lshl_add_u64 v[232:233], s[24:25], 0, v[178:179]
	ds_read_b128 v[216:219], v183
	ds_read_b128 v[220:223], v183 offset:1024
	ds_read_b128 v[224:227], v183 offset:2048
	ds_read_b128 v[228:231], v183 offset:3072
	global_load_lds_dwordx4 v[232:233], off
	v_lshl_add_u64 v[234:235], s[24:25], 0, v[180:181]
	s_mov_b32 m0, s44
	s_nop 0
	global_load_lds_dwordx4 v[234:235], off
	s_setprio 1
	s_barrier
	s_waitcnt lgkmcnt(0)
	v_mfma_f32_16x16x32_bf16 v[118:121], v[216:219], v[170:173], v[118:121]
	v_mfma_f32_16x16x32_bf16 v[114:117], v[224:227], v[170:173], v[114:117]
	v_mfma_f32_16x16x32_bf16 v[102:105], v[216:219], v[162:165], v[102:105]
	v_mfma_f32_16x16x32_bf16 v[98:101], v[224:227], v[162:165], v[98:101]
	v_mfma_f32_16x16x32_bf16 v[86:89], v[216:219], v[154:157], v[86:89]
	v_mfma_f32_16x16x32_bf16 v[82:85], v[224:227], v[154:157], v[82:85]
	v_mfma_f32_16x16x32_bf16 v[70:73], v[216:219], v[146:149], v[70:73]
	v_mfma_f32_16x16x32_bf16 v[66:69], v[224:227], v[146:149], v[66:69]
	v_mfma_f32_16x16x32_bf16 v[118:121], v[220:223], v[174:177], v[118:121]
	s_mov_b32 m0, s42
	v_mfma_f32_16x16x32_bf16 v[114:117], v[228:231], v[174:177], v[114:117]
	v_mfma_f32_16x16x32_bf16 v[102:105], v[220:223], v[166:169], v[102:105]
	v_mfma_f32_16x16x32_bf16 v[98:101], v[228:231], v[166:169], v[98:101]
	v_mfma_f32_16x16x32_bf16 v[86:89], v[220:223], v[158:161], v[86:89]
	v_mfma_f32_16x16x32_bf16 v[82:85], v[228:231], v[158:161], v[82:85]
	v_mfma_f32_16x16x32_bf16 v[70:73], v[220:223], v[150:153], v[70:73]
	v_mfma_f32_16x16x32_bf16 v[66:69], v[228:231], v[150:153], v[66:69]
	s_setprio 0
	s_barrier
	ds_read_b128 v[146:149], v200 offset:16384
	ds_read_b128 v[150:153], v200 offset:17408
	ds_read_b128 v[154:157], v200 offset:18432
	ds_read_b128 v[158:161], v200 offset:19456
	ds_read_b128 v[162:165], v200 offset:20480
	ds_read_b128 v[166:169], v200 offset:21504
	ds_read_b128 v[170:173], v200 offset:22528
	ds_read_b128 v[174:177], v200 offset:23552
	global_load_lds_dwordx4 v0, s[34:35]
	s_mov_b32 m0, s45
	v_mov_b32_e32 v183, v1
	global_load_lds_dwordx4 v182, s[34:35]
	s_barrier
	s_waitcnt lgkmcnt(0)
	v_lshl_add_u64 v[236:237], s[34:35], 0, v[0:1]
	v_lshl_add_u64 v[238:239], s[34:35], 0, v[182:183]
	s_setprio 1
	s_waitcnt lgkmcnt(0)
	v_mfma_f32_16x16x32_bf16 v[62:65], v[130:133], v[146:149], v[62:65]
	v_mfma_f32_16x16x32_bf16 v[58:61], v[138:141], v[146:149], v[58:61]
	v_mfma_f32_16x16x32_bf16 v[46:49], v[130:133], v[154:157], v[46:49]
	v_mfma_f32_16x16x32_bf16 v[42:45], v[138:141], v[154:157], v[42:45]
	v_mfma_f32_16x16x32_bf16 v[30:33], v[130:133], v[162:165], v[30:33]
	v_mfma_f32_16x16x32_bf16 v[26:29], v[138:141], v[162:165], v[26:29]
	v_mfma_f32_16x16x32_bf16 v[14:17], v[130:133], v[170:173], v[14:17]
	v_mfma_f32_16x16x32_bf16 v[10:13], v[138:141], v[170:173], v[10:13]
	v_mfma_f32_16x16x32_bf16 v[62:65], v[134:137], v[150:153], v[62:65]
	v_mfma_f32_16x16x32_bf16 v[58:61], v[142:145], v[150:153], v[58:61]
	v_mfma_f32_16x16x32_bf16 v[46:49], v[134:137], v[158:161], v[46:49]
	v_mfma_f32_16x16x32_bf16 v[42:45], v[142:145], v[158:161], v[42:45]
	v_mfma_f32_16x16x32_bf16 v[30:33], v[134:137], v[166:169], v[30:33]
	v_mfma_f32_16x16x32_bf16 v[26:29], v[142:145], v[166:169], v[26:29]
	v_mfma_f32_16x16x32_bf16 v[14:17], v[134:137], v[174:177], v[14:17]
	v_mfma_f32_16x16x32_bf16 v[10:13], v[142:145], v[174:177], v[10:13]
	s_setprio 0
	s_barrier
	s_add_u32 s58, s24, 0x40000
	s_addc_u32 s59, s25, 0
	s_add_i32 s60, s60, s41
	v_lshl_add_u64 v[130:131], s[58:59], 0, v[178:179]
	s_mov_b32 m0, s60
	s_nop 0
	global_load_lds_dwordx4 v[130:131], off
	v_lshl_add_u64 v[130:131], s[58:59], 0, v[180:181]
	s_add_i32 m0, s60, 0x2000
	s_nop 0
	global_load_lds_dwordx4 v[130:131], off
	s_waitcnt vmcnt(6)
	s_setprio 1
	s_barrier
; #define G8_STAGE(bufoff, gbase, voff) do { _Pragma("unroll") for (int _i = 0; _i < 2; ++_i) \
;         __builtin_amdgcn_global_load_lds((const unsigned*)((const char*)(gbase) + (voff)[_i]), (LAS unsigned*)(lds + (bufoff) + ldsw + _i * 8192), 16, 0, 0); } while (0)
; #define G8_LDA(dst, b, h) do { _Pragma("unroll") for (int m = 0; m < 4; ++m) _Pragma("unroll") for (int k = 0; k < 2; ++k) dst[m][k] = *(const LAS bf16x8*)(lds + G8_SA(b, h) + aoff + m * 2048 + k * 1024); } while (0)
; #define G8_LDB(dst, b, h) do { _Pragma("unroll") for (int n = 0; n < 2; ++n) _Pragma("unroll") for (int k = 0; k < 2; ++k) dst[n][k] = *(const LAS bf16x8*)(lds + G8_SB(b, h) + boff + n * 2048 + k * 1024); } while (0)
; #define G8_MMA(ai, bj, At, Bt) do { __builtin_amdgcn_s_setprio(1); _Pragma("unroll") for (int m = 0; m < 4; ++m) _Pragma("unroll") for (int n = 0; n < 2; ++n) _Pragma("unroll") for (int k = 0; k < 2; ++k) \
;         acc[ai][bj][m][n] = __builtin_amdgcn_mfma_f32_16x16x32_bf16(Bt[n][k], At[m][k], acc[ai][bj][m][n], 0, 0, 0); __builtin_amdgcn_s_setprio(0); } while (0)
; #define G8_WAIT_V(n) asm volatile("s_waitcnt vmcnt(" #n ")" ::: "memory")
; #define G8_WAIT_L(n) asm volatile("s_waitcnt lgkmcnt(" #n ")" ::: "memory")
; #define G8_BAR __builtin_amdgcn_s_barrier()
; #define G8_SCHED __builtin_amdgcn_sched_barrier(0)
; template <class Epi, class Sched>
; __device__ __forceinline__ void gemm_phase(LAS unsigned char* lds, const int K, const Sched& S, const Epi& E) {
;     ...
;             G8_WAIT_V(6); G8_BAR; G8_MMA(1, 1, At, B1); G8_BAR;
;             G8_LDB(B0, 1, 0); G8_SCHED; G8_LDA(At, 1, 0); G8_STAGE(G8_SA(0, 1), a2, oc[1]);
;             G8_WAIT_L(8); G8_BAR; G8_WAIT_L(0); G8_MMA(0, 0, At, B0); G8_BAR; G8_SCHED;
;             G8_LDB(B1, 1, 1); G8_STAGE(G8_SB(1, 0), b3, voffB);
;             G8_BAR; G8_WAIT_L(0); G8_MMA(0, 1, At, B1); G8_BAR;
	v_mfma_f32_16x16x32_bf16 v[54:57], v[216:219], v[146:149], v[54:57]
	v_mfma_f32_16x16x32_bf16 v[50:53], v[224:227], v[146:149], v[50:53]
	v_mfma_f32_16x16x32_bf16 v[38:41], v[216:219], v[154:157], v[38:41]
	v_mfma_f32_16x16x32_bf16 v[34:37], v[224:227], v[154:157], v[34:37]
	v_mfma_f32_16x16x32_bf16 v[22:25], v[216:219], v[162:165], v[22:25]
	v_mfma_f32_16x16x32_bf16 v[18:21], v[224:227], v[162:165], v[18:21]
	v_mfma_f32_16x16x32_bf16 v[6:9], v[216:219], v[170:173], v[6:9]
	v_mfma_f32_16x16x32_bf16 v[2:5], v[224:227], v[170:173], v[2:5]
	v_mfma_f32_16x16x32_bf16 v[54:57], v[220:223], v[150:153], v[54:57]
	s_add_i32 s58, 0, 0x18000
	v_mfma_f32_16x16x32_bf16 v[50:53], v[228:231], v[150:153], v[50:53]
	v_add_u32_e32 v142, s58, v198
	v_mfma_f32_16x16x32_bf16 v[38:41], v[220:223], v[158:161], v[38:41]
	v_mfma_f32_16x16x32_bf16 v[34:37], v[228:231], v[158:161], v[34:37]
	v_mfma_f32_16x16x32_bf16 v[22:25], v[220:223], v[166:169], v[22:25]
	v_mfma_f32_16x16x32_bf16 v[18:21], v[228:231], v[166:169], v[18:21]
	v_mfma_f32_16x16x32_bf16 v[6:9], v[220:223], v[174:177], v[6:9]
	v_mfma_f32_16x16x32_bf16 v[2:5], v[228:231], v[174:177], v[2:5]
	s_setprio 0
	s_barrier
	ds_read_b128 v[130:133], v142
	ds_read_b128 v[134:137], v142 offset:1024
	ds_read_b128 v[138:141], v142 offset:2048
	ds_read_b128 v[142:145], v142 offset:3072
	s_mov_b32 m0, s46
	v_lshl_add_u64 v[190:191], s[34:35], 0, v[190:191]
	ds_read_b128 v[146:149], v200 offset:32768
	ds_read_b128 v[150:153], v200 offset:33792
	ds_read_b128 v[154:157], v200 offset:34816
	ds_read_b128 v[158:161], v200 offset:35840
	ds_read_b128 v[162:165], v200 offset:36864
	ds_read_b128 v[166:169], v200 offset:37888
	ds_read_b128 v[170:173], v200 offset:38912
	ds_read_b128 v[174:177], v200 offset:39936
	global_load_lds_dwordx4 v[190:191], off
	v_lshl_add_u64 v[190:191], s[34:35], 0, v[186:187]
	s_mov_b32 m0, s47
	s_nop 0
	global_load_lds_dwordx4 v[190:191], off
	s_waitcnt lgkmcnt(8)
	s_setprio 1
	s_barrier
	s_waitcnt lgkmcnt(0)
	v_mfma_f32_16x16x32_bf16 v[126:129], v[130:133], v[146:149], v[126:129]
	v_mfma_f32_16x16x32_bf16 v[122:125], v[138:141], v[146:149], v[122:125]
	v_mfma_f32_16x16x32_bf16 v[110:113], v[130:133], v[154:157], v[110:113]
	v_mfma_f32_16x16x32_bf16 v[106:109], v[138:141], v[154:157], v[106:109]
	v_mfma_f32_16x16x32_bf16 v[94:97], v[130:133], v[162:165], v[94:97]
	v_mfma_f32_16x16x32_bf16 v[90:93], v[138:141], v[162:165], v[90:93]
	v_mfma_f32_16x16x32_bf16 v[78:81], v[130:133], v[170:173], v[78:81]
	v_mfma_f32_16x16x32_bf16 v[74:77], v[138:141], v[170:173], v[74:77]
	v_mfma_f32_16x16x32_bf16 v[126:129], v[134:137], v[150:153], v[126:129]
	v_mfma_f32_16x16x32_bf16 v[122:125], v[142:145], v[150:153], v[122:125]
	v_mfma_f32_16x16x32_bf16 v[110:113], v[134:137], v[158:161], v[110:113]
	v_mfma_f32_16x16x32_bf16 v[106:109], v[142:145], v[158:161], v[106:109]
	v_mfma_f32_16x16x32_bf16 v[94:97], v[134:137], v[166:169], v[94:97]
	v_mfma_f32_16x16x32_bf16 v[90:93], v[142:145], v[166:169], v[90:93]
	v_mfma_f32_16x16x32_bf16 v[78:81], v[134:137], v[174:177], v[78:81]
	v_mfma_f32_16x16x32_bf16 v[74:77], v[142:145], v[174:177], v[74:77]
	s_setprio 0
	s_barrier
	s_add_i32 s34, 0, 0x1c000
	s_add_i32 s35, s58, s41
	v_add_u32_e32 v183, s34, v198
	v_lshl_add_u64 v[190:191], v[232:233], 0, s[18:19]
	s_mov_b32 m0, s35
	ds_read_b128 v[216:219], v183
	ds_read_b128 v[220:223], v183 offset:1024
	ds_read_b128 v[224:227], v183 offset:2048
	ds_read_b128 v[228:231], v183 offset:3072
	global_load_lds_dwordx4 v[190:191], off
	v_lshl_add_u64 v[190:191], v[234:235], 0, s[18:19]
	s_add_i32 m0, s35, 0x2000
	s_nop 0
	global_load_lds_dwordx4 v[190:191], off
	s_setprio 1
	s_barrier
; #define G8_STAGE(bufoff, gbase, voff) do { _Pragma("unroll") for (int _i = 0; _i < 2; ++_i) \
;         __builtin_amdgcn_global_load_lds((const unsigned*)((const char*)(gbase) + (voff)[_i]), (LAS unsigned*)(lds + (bufoff) + ldsw + _i * 8192), 16, 0, 0); } while (0)
; #define G8_LDA(dst, b, h) do { _Pragma("unroll") for (int m = 0; m < 4; ++m) _Pragma("unroll") for (int k = 0; k < 2; ++k) dst[m][k] = *(const LAS bf16x8*)(lds + G8_SA(b, h) + aoff + m * 2048 + k * 1024); } while (0)
; #define G8_MMA(ai, bj, At, Bt) do { __builtin_amdgcn_s_setprio(1); _Pragma("unroll") for (int m = 0; m < 4; ++m) _Pragma("unroll") for (int n = 0; n < 2; ++n) _Pragma("unroll") for (int k = 0; k < 2; ++k) \
;         acc[ai][bj][m][n] = __builtin_amdgcn_mfma_f32_16x16x32_bf16(Bt[n][k], At[m][k], acc[ai][bj][m][n], 0, 0, 0); __builtin_amdgcn_s_setprio(0); } while (0)
; #define G8_WAIT_V(n) asm volatile("s_waitcnt vmcnt(" #n ")" ::: "memory")
; #define G8_WAIT_L(n) asm volatile("s_waitcnt lgkmcnt(" #n ")" ::: "memory")
; #define G8_BAR __builtin_amdgcn_s_barrier()
; #define G8_SCHED __builtin_amdgcn_sched_barrier(0)
; template <class Epi, class Sched>
; __device__ __forceinline__ void gemm_phase(LAS unsigned char* lds, const int K, const Sched& S, const Epi& E) {
;     ...
;             G8_BAR; G8_WAIT_L(0); G8_MMA(0, 1, At, B1); G8_BAR;
;             G8_LDA(At, 1, 1); G8_STAGE(G8_SA(1, 0), a3, oc[0]);
;             G8_BAR; G8_WAIT_L(0); G8_MMA(1, 0, At, B0); G8_BAR; G8_SCHED;
;             G8_STAGE(G8_SB(1, 1), b3 + hstep, voffB);
;             G8_WAIT_V(6); G8_BAR; G8_MMA(1, 1, At, B1); G8_BAR;
	s_waitcnt lgkmcnt(0)
	v_mfma_f32_16x16x32_bf16 v[118:121], v[216:219], v[146:149], v[118:121]
	v_mfma_f32_16x16x32_bf16 v[114:117], v[224:227], v[146:149], v[114:117]
	v_mfma_f32_16x16x32_bf16 v[102:105], v[216:219], v[154:157], v[102:105]
	v_mfma_f32_16x16x32_bf16 v[98:101], v[224:227], v[154:157], v[98:101]
	v_mfma_f32_16x16x32_bf16 v[86:89], v[216:219], v[162:165], v[86:89]
	v_mfma_f32_16x16x32_bf16 v[82:85], v[224:227], v[162:165], v[82:85]
	v_mfma_f32_16x16x32_bf16 v[70:73], v[216:219], v[170:173], v[70:73]
	v_mfma_f32_16x16x32_bf16 v[66:69], v[224:227], v[170:173], v[66:69]
	v_mfma_f32_16x16x32_bf16 v[118:121], v[220:223], v[150:153], v[118:121]
	s_mov_b32 m0, s49
	v_mfma_f32_16x16x32_bf16 v[114:117], v[228:231], v[150:153], v[114:117]
	v_lshl_add_u64 v[190:191], v[236:237], 0, s[18:19]
	v_mfma_f32_16x16x32_bf16 v[102:105], v[220:223], v[158:161], v[102:105]
	v_mfma_f32_16x16x32_bf16 v[98:101], v[228:231], v[158:161], v[98:101]
	v_mfma_f32_16x16x32_bf16 v[86:89], v[220:223], v[166:169], v[86:89]
	v_mfma_f32_16x16x32_bf16 v[82:85], v[228:231], v[166:169], v[82:85]
	v_mfma_f32_16x16x32_bf16 v[70:73], v[220:223], v[174:177], v[70:73]
	v_mfma_f32_16x16x32_bf16 v[66:69], v[228:231], v[174:177], v[66:69]
	s_setprio 0
	s_barrier
	ds_read_b128 v[146:149], v200 offset:49152
	ds_read_b128 v[150:153], v200 offset:50176
	ds_read_b128 v[154:157], v200 offset:51200
	ds_read_b128 v[158:161], v200 offset:52224
	ds_read_b128 v[162:165], v200 offset:53248
	ds_read_b128 v[166:169], v200 offset:54272
	ds_read_b128 v[170:173], v200 offset:55296
	ds_read_b128 v[174:177], v200 offset:56320
	global_load_lds_dwordx4 v[190:191], off
	v_lshl_add_u64 v[190:191], v[238:239], 0, s[18:19]
	s_mov_b32 m0, s50
	s_nop 0
	global_load_lds_dwordx4 v[190:191], off
	s_setprio 1
	s_barrier
	s_waitcnt lgkmcnt(0)
	v_mfma_f32_16x16x32_bf16 v[62:65], v[130:133], v[146:149], v[62:65]
	v_mfma_f32_16x16x32_bf16 v[58:61], v[138:141], v[146:149], v[58:61]
	v_mfma_f32_16x16x32_bf16 v[46:49], v[130:133], v[154:157], v[46:49]
	v_mfma_f32_16x16x32_bf16 v[42:45], v[138:141], v[154:157], v[42:45]
	v_mfma_f32_16x16x32_bf16 v[30:33], v[130:133], v[162:165], v[30:33]
	v_mfma_f32_16x16x32_bf16 v[26:29], v[138:141], v[162:165], v[26:29]
	v_mfma_f32_16x16x32_bf16 v[14:17], v[130:133], v[170:173], v[14:17]
	v_mfma_f32_16x16x32_bf16 v[10:13], v[138:141], v[170:173], v[10:13]
	v_mfma_f32_16x16x32_bf16 v[62:65], v[134:137], v[150:153], v[62:65]
	v_mfma_f32_16x16x32_bf16 v[58:61], v[142:145], v[150:153], v[58:61]
	v_mfma_f32_16x16x32_bf16 v[46:49], v[134:137], v[158:161], v[46:49]
	v_mfma_f32_16x16x32_bf16 v[42:45], v[142:145], v[158:161], v[42:45]
	v_mfma_f32_16x16x32_bf16 v[30:33], v[134:137], v[166:169], v[30:33]
	v_mfma_f32_16x16x32_bf16 v[26:29], v[142:145], v[166:169], v[26:29]
	v_mfma_f32_16x16x32_bf16 v[14:17], v[134:137], v[174:177], v[14:17]
	v_mfma_f32_16x16x32_bf16 v[10:13], v[142:145], v[174:177], v[10:13]
	s_setprio 0
	s_barrier
	s_add_u32 s24, s24, 0x40080
	s_addc_u32 s25, s25, 0
	s_add_i32 s34, s34, s41
	v_lshl_add_u64 v[130:131], s[24:25], 0, v[178:179]
	s_mov_b32 m0, s34
	s_nop 0
	global_load_lds_dwordx4 v[130:131], off
	v_lshl_add_u64 v[130:131], s[24:25], 0, v[180:181]
	s_add_i32 m0, s34, 0x2000
	s_nop 0
	global_load_lds_dwordx4 v[130:131], off
	s_waitcnt vmcnt(6)
	s_setprio 1
	s_barrier
	v_mfma_f32_16x16x32_bf16 v[54:57], v[216:219], v[146:149], v[54:57]
	v_mfma_f32_16x16x32_bf16 v[50:53], v[224:227], v[146:149], v[50:53]
	v_mfma_f32_16x16x32_bf16 v[38:41], v[216:219], v[154:157], v[38:41]
	v_mfma_f32_16x16x32_bf16 v[34:37], v[224:227], v[154:157], v[34:37]
	v_mfma_f32_16x16x32_bf16 v[22:25], v[216:219], v[162:165], v[22:25]
	v_mfma_f32_16x16x32_bf16 v[18:21], v[224:227], v[162:165], v[18:21]
	v_mfma_f32_16x16x32_bf16 v[6:9], v[216:219], v[170:173], v[6:9]
	v_mfma_f32_16x16x32_bf16 v[2:5], v[224:227], v[170:173], v[2:5]
	v_mfma_f32_16x16x32_bf16 v[54:57], v[220:223], v[150:153], v[54:57]
	s_add_i32 s57, s57, 2
	v_mfma_f32_16x16x32_bf16 v[50:53], v[228:231], v[150:153], v[50:53]
	s_add_u32 s22, s22, 0x100
	v_mfma_f32_16x16x32_bf16 v[38:41], v[220:223], v[158:161], v[38:41]
	s_addc_u32 s23, s23, 0
	v_mfma_f32_16x16x32_bf16 v[34:37], v[228:231], v[158:161], v[34:37]
	s_add_u32 s55, s55, 0x100
	v_mfma_f32_16x16x32_bf16 v[22:25], v[220:223], v[166:169], v[22:25]
	s_addc_u32 s56, s56, 0
	v_mfma_f32_16x16x32_bf16 v[18:21], v[228:231], v[166:169], v[18:21]
	s_cmp_gt_u32 s57, 13
	v_mfma_f32_16x16x32_bf16 v[6:9], v[220:223], v[174:177], v[6:9]
	v_mfma_f32_16x16x32_bf16 v[2:5], v[228:231], v[174:177], v[2:5]
	s_setprio 0
	s_barrier
	s_cbranch_scc1 .LBB0_2529

; #define G8_STAGE(bufoff, gbase, voff) do { _Pragma("unroll") for (int _i = 0; _i < 2; ++_i) \
;         __builtin_amdgcn_global_load_lds((const unsigned*)((const char*)(gbase) + (voff)[_i]), (LAS unsigned*)(lds + (bufoff) + ldsw + _i * 8192), 16, 0, 0); } while (0)
; #define G8_LDA(dst, b, h) do { _Pragma("unroll") for (int m = 0; m < 4; ++m) _Pragma("unroll") for (int k = 0; k < 2; ++k) dst[m][k] = *(const LAS bf16x8*)(lds + G8_SA(b, h) + aoff + m * 2048 + k * 1024); } while (0)
; #define G8_LDB(dst, b, h) do { _Pragma("unroll") for (int n = 0; n < 2; ++n) _Pragma("unroll") for (int k = 0; k < 2; ++k) dst[n][k] = *(const LAS bf16x8*)(lds + G8_SB(b, h) + boff + n * 2048 + k * 1024); } while (0)
; #define G8_MMA(ai, bj, At, Bt) do { __builtin_amdgcn_s_setprio(1); _Pragma("unroll") for (int m = 0; m < 4; ++m) _Pragma("unroll") for (int n = 0; n < 2; ++n) _Pragma("unroll") for (int k = 0; k < 2; ++k) \
;         acc[ai][bj][m][n] = __builtin_amdgcn_mfma_f32_16x16x32_bf16(Bt[n][k], At[m][k], acc[ai][bj][m][n], 0, 0, 0); __builtin_amdgcn_s_setprio(0); } while (0)
; #define G8_WAIT_V(n) asm volatile("s_waitcnt vmcnt(" #n ")" ::: "memory")
; #define G8_WAIT_L(n) asm volatile("s_waitcnt lgkmcnt(" #n ")" ::: "memory")
; #define G8_BAR __builtin_amdgcn_s_barrier()
; #define G8_SCHED __builtin_amdgcn_sched_barrier(0)
; template <class Epi, class Sched>
; __device__ __forceinline__ void gemm_phase(LAS unsigned char* lds, const int K, const Sched& S, const Epi& E) {
;     ...
;             const char* a1 = cA + (size_t)(t + 1) * kstep;
;             const char* a2 = last ? nA : cA + (size_t)(t + 2) * kstep; const char* b2 = last ? nB : cB + (size_t)(t + 2) * kstep;
;             const char* a3 = a2 + kstep; const char* b3 = b2 + kstep;
;             G8_LDB(B0, 0, 0); G8_SCHED; G8_LDA(At, 0, 0); G8_STAGE(G8_SA(1, 1), a1, oc[1]);
;             if (last && has_next) S.aoff(nxt, tid, oc);
;             G8_WAIT_L(8); G8_BAR; G8_WAIT_L(0); G8_MMA(0, 0, At, B0); G8_BAR; G8_SCHED;
;             G8_LDB(B1, 0, 1); G8_STAGE(G8_SB(0, 0), b2, voffB);
;             G8_BAR; G8_WAIT_L(0); G8_MMA(0, 1, At, B1); G8_BAR;
;             G8_LDA(At, 0, 1); G8_STAGE(G8_SA(0, 0), a2, oc[0]);
;             G8_BAR; G8_WAIT_L(0); G8_MMA(1, 0, At, B0); G8_BAR; G8_SCHED;
;             G8_STAGE(G8_SB(0, 1), b2 + hstep, voffB);
;             G8_WAIT_V(6); G8_BAR; G8_MMA(1, 1, At, B1); G8_BAR;
.LBB0_2616:
	s_xor_b64 s[40:41], s[42:43], -1
	s_add_u32 s44, s44, 0x100
	s_addc_u32 s45, s45, 0
	s_and_b64 s[42:43], s[36:37], exec
	s_cselect_b32 s43, s1, s45
	s_cselect_b32 s42, s0, s44
	s_add_u32 s38, s22, s38
	s_addc_u32 s39, s23, s39
	s_add_u32 s38, s38, 0x100
	s_addc_u32 s39, s39, 0
	s_and_b64 s[36:37], s[36:37], exec
	s_cselect_b32 s37, s35, s39
	s_cselect_b32 s36, s34, s38
	s_setprio 1
	s_waitcnt lgkmcnt(8)
	s_barrier
	s_waitcnt lgkmcnt(0)
	s_waitcnt lgkmcnt(0)
	v_mfma_f32_16x16x32_bf16 v[126:129], v[130:133], v[170:173], v[126:129]
	v_mfma_f32_16x16x32_bf16 v[122:125], v[138:141], v[170:173], v[122:125]
	v_mfma_f32_16x16x32_bf16 v[110:113], v[130:133], v[162:165], v[110:113]
	v_mfma_f32_16x16x32_bf16 v[106:109], v[138:141], v[162:165], v[106:109]
	v_mfma_f32_16x16x32_bf16 v[94:97], v[130:133], v[154:157], v[94:97]
	v_mfma_f32_16x16x32_bf16 v[90:93], v[138:141], v[154:157], v[90:93]
	v_mfma_f32_16x16x32_bf16 v[78:81], v[130:133], v[146:149], v[78:81]
	v_mfma_f32_16x16x32_bf16 v[74:77], v[138:141], v[146:149], v[74:77]
	v_mfma_f32_16x16x32_bf16 v[126:129], v[134:137], v[174:177], v[126:129]
	v_mfma_f32_16x16x32_bf16 v[122:125], v[142:145], v[174:177], v[122:125]
	v_mfma_f32_16x16x32_bf16 v[110:113], v[134:137], v[166:169], v[110:113]
	v_mfma_f32_16x16x32_bf16 v[106:109], v[142:145], v[166:169], v[106:109]
	v_mfma_f32_16x16x32_bf16 v[94:97], v[134:137], v[158:161], v[94:97]
	v_mfma_f32_16x16x32_bf16 v[90:93], v[142:145], v[158:161], v[90:93]
	v_mfma_f32_16x16x32_bf16 v[78:81], v[134:137], v[150:153], v[78:81]
	v_mfma_f32_16x16x32_bf16 v[74:77], v[142:145], v[150:153], v[74:77]
	s_setprio 0
	s_barrier
	s_add_i32 s44, 0, 0x14000
	s_mov_b32 m0, s52
	v_add_u32_e32 v183, s44, v200
	v_lshl_add_u64 v[236:237], s[36:37], 0, v[178:179]
	ds_read_b128 v[220:223], v183
	ds_read_b128 v[224:227], v183 offset:1024
	ds_read_b128 v[228:231], v183 offset:2048
	ds_read_b128 v[232:235], v183 offset:3072
	global_load_lds_dwordx4 v[236:237], off
	v_lshl_add_u64 v[238:239], s[36:37], 0, v[180:181]
	s_mov_b32 m0, s53
	s_nop 0
	global_load_lds_dwordx4 v[238:239], off
	s_setprio 1
	s_barrier
	s_waitcnt lgkmcnt(0)
	v_mfma_f32_16x16x32_bf16 v[118:121], v[220:223], v[170:173], v[118:121]
	v_mfma_f32_16x16x32_bf16 v[114:117], v[228:231], v[170:173], v[114:117]
	v_mfma_f32_16x16x32_bf16 v[102:105], v[220:223], v[162:165], v[102:105]
	v_mfma_f32_16x16x32_bf16 v[98:101], v[228:231], v[162:165], v[98:101]
	v_mfma_f32_16x16x32_bf16 v[86:89], v[220:223], v[154:157], v[86:89]
	v_mfma_f32_16x16x32_bf16 v[82:85], v[228:231], v[154:157], v[82:85]
	v_mfma_f32_16x16x32_bf16 v[70:73], v[220:223], v[146:149], v[70:73]
	v_mfma_f32_16x16x32_bf16 v[66:69], v[228:231], v[146:149], v[66:69]
	v_mfma_f32_16x16x32_bf16 v[118:121], v[224:227], v[174:177], v[118:121]
	s_mov_b32 m0, s51
	v_mfma_f32_16x16x32_bf16 v[114:117], v[232:235], v[174:177], v[114:117]
	v_mfma_f32_16x16x32_bf16 v[102:105], v[224:227], v[166:169], v[102:105]
	v_mfma_f32_16x16x32_bf16 v[98:101], v[232:235], v[166:169], v[98:101]
	v_mfma_f32_16x16x32_bf16 v[86:89], v[224:227], v[158:161], v[86:89]
	v_mfma_f32_16x16x32_bf16 v[82:85], v[232:235], v[158:161], v[82:85]
	v_mfma_f32_16x16x32_bf16 v[70:73], v[224:227], v[150:153], v[70:73]
	v_mfma_f32_16x16x32_bf16 v[66:69], v[232:235], v[150:153], v[66:69]
	s_setprio 0
	s_barrier
	ds_read_b128 v[146:149], v216 offset:16384
	ds_read_b128 v[150:153], v216 offset:17408
	ds_read_b128 v[154:157], v216 offset:18432
	ds_read_b128 v[158:161], v216 offset:19456
	ds_read_b128 v[162:165], v216 offset:20480
	ds_read_b128 v[166:169], v216 offset:21504
	ds_read_b128 v[170:173], v216 offset:22528
	ds_read_b128 v[174:177], v216 offset:23552
	global_load_lds_dwordx4 v182, s[42:43]
	s_mov_b32 m0, s54
	v_mov_b32_e32 v183, v1
	global_load_lds_dwordx4 v184, s[42:43]
	s_barrier
	s_waitcnt lgkmcnt(0)
	v_mov_b32_e32 v185, v1
	v_lshl_add_u64 v[240:241], s[42:43], 0, v[182:183]
	v_lshl_add_u64 v[242:243], s[42:43], 0, v[184:185]
	s_setprio 1
	s_waitcnt lgkmcnt(0)
	v_mfma_f32_16x16x32_bf16 v[62:65], v[130:133], v[146:149], v[62:65]
	v_mfma_f32_16x16x32_bf16 v[58:61], v[138:141], v[146:149], v[58:61]
	v_mfma_f32_16x16x32_bf16 v[46:49], v[130:133], v[154:157], v[46:49]
	v_mfma_f32_16x16x32_bf16 v[42:45], v[138:141], v[154:157], v[42:45]
	v_mfma_f32_16x16x32_bf16 v[30:33], v[130:133], v[162:165], v[30:33]
	v_mfma_f32_16x16x32_bf16 v[26:29], v[138:141], v[162:165], v[26:29]
	v_mfma_f32_16x16x32_bf16 v[14:17], v[130:133], v[170:173], v[14:17]
	v_mfma_f32_16x16x32_bf16 v[10:13], v[138:141], v[170:173], v[10:13]
	v_mfma_f32_16x16x32_bf16 v[62:65], v[134:137], v[150:153], v[62:65]
	v_mfma_f32_16x16x32_bf16 v[58:61], v[142:145], v[150:153], v[58:61]
	v_mfma_f32_16x16x32_bf16 v[46:49], v[134:137], v[158:161], v[46:49]
	v_mfma_f32_16x16x32_bf16 v[42:45], v[142:145], v[158:161], v[42:45]
	v_mfma_f32_16x16x32_bf16 v[30:33], v[134:137], v[166:169], v[30:33]
	v_mfma_f32_16x16x32_bf16 v[26:29], v[142:145], v[166:169], v[26:29]
	v_mfma_f32_16x16x32_bf16 v[14:17], v[134:137], v[174:177], v[14:17]
	v_mfma_f32_16x16x32_bf16 v[10:13], v[142:145], v[174:177], v[10:13]
	s_setprio 0
	s_barrier
	s_add_u32 s38, s36, 0x10000
	s_addc_u32 s39, s37, 0
	s_add_i32 s44, s44, s50
	v_lshl_add_u64 v[130:131], s[38:39], 0, v[178:179]
	s_mov_b32 m0, s44
	s_nop 0
	global_load_lds_dwordx4 v[130:131], off
	v_lshl_add_u64 v[130:131], s[38:39], 0, v[180:181]
	s_add_i32 m0, s44, 0x2000
	s_nop 0
	global_load_lds_dwordx4 v[130:131], off
	s_waitcnt vmcnt(6)
	s_setprio 1
	s_barrier
; #define G8_STAGE(bufoff, gbase, voff) do { _Pragma("unroll") for (int _i = 0; _i < 2; ++_i) \
;         __builtin_amdgcn_global_load_lds((const unsigned*)((const char*)(gbase) + (voff)[_i]), (LAS unsigned*)(lds + (bufoff) + ldsw + _i * 8192), 16, 0, 0); } while (0)
; #define G8_LDA(dst, b, h) do { _Pragma("unroll") for (int m = 0; m < 4; ++m) _Pragma("unroll") for (int k = 0; k < 2; ++k) dst[m][k] = *(const LAS bf16x8*)(lds + G8_SA(b, h) + aoff + m * 2048 + k * 1024); } while (0)
; #define G8_LDB(dst, b, h) do { _Pragma("unroll") for (int n = 0; n < 2; ++n) _Pragma("unroll") for (int k = 0; k < 2; ++k) dst[n][k] = *(const LAS bf16x8*)(lds + G8_SB(b, h) + boff + n * 2048 + k * 1024); } while (0)
; #define G8_MMA(ai, bj, At, Bt) do { __builtin_amdgcn_s_setprio(1); _Pragma("unroll") for (int m = 0; m < 4; ++m) _Pragma("unroll") for (int n = 0; n < 2; ++n) _Pragma("unroll") for (int k = 0; k < 2; ++k) \
;         acc[ai][bj][m][n] = __builtin_amdgcn_mfma_f32_16x16x32_bf16(Bt[n][k], At[m][k], acc[ai][bj][m][n], 0, 0, 0); __builtin_amdgcn_s_setprio(0); } while (0)
; #define G8_WAIT_V(n) asm volatile("s_waitcnt vmcnt(" #n ")" ::: "memory")
; #define G8_WAIT_L(n) asm volatile("s_waitcnt lgkmcnt(" #n ")" ::: "memory")
; #define G8_BAR __builtin_amdgcn_s_barrier()
; #define G8_SCHED __builtin_amdgcn_sched_barrier(0)
; template <class Epi, class Sched>
; __device__ __forceinline__ void gemm_phase(LAS unsigned char* lds, const int K, const Sched& S, const Epi& E) {
;     ...
;             G8_WAIT_V(6); G8_BAR; G8_MMA(1, 1, At, B1); G8_BAR;
;             G8_LDB(B0, 1, 0); G8_SCHED; G8_LDA(At, 1, 0); G8_STAGE(G8_SA(0, 1), a2, oc[1]);
;             G8_WAIT_L(8); G8_BAR; G8_WAIT_L(0); G8_MMA(0, 0, At, B0); G8_BAR; G8_SCHED;
;             G8_LDB(B1, 1, 1); G8_STAGE(G8_SB(1, 0), b3, voffB);
;             G8_BAR; G8_WAIT_L(0); G8_MMA(0, 1, At, B1); G8_BAR;
	v_mfma_f32_16x16x32_bf16 v[54:57], v[220:223], v[146:149], v[54:57]
	v_mfma_f32_16x16x32_bf16 v[50:53], v[228:231], v[146:149], v[50:53]
	v_mfma_f32_16x16x32_bf16 v[38:41], v[220:223], v[154:157], v[38:41]
	v_mfma_f32_16x16x32_bf16 v[34:37], v[228:231], v[154:157], v[34:37]
	v_mfma_f32_16x16x32_bf16 v[22:25], v[220:223], v[162:165], v[22:25]
	v_mfma_f32_16x16x32_bf16 v[18:21], v[228:231], v[162:165], v[18:21]
	v_mfma_f32_16x16x32_bf16 v[6:9], v[220:223], v[170:173], v[6:9]
	v_mfma_f32_16x16x32_bf16 v[2:5], v[228:231], v[170:173], v[2:5]
	v_mfma_f32_16x16x32_bf16 v[54:57], v[224:227], v[150:153], v[54:57]
	s_add_i32 s38, 0, 0x18000
	v_mfma_f32_16x16x32_bf16 v[50:53], v[232:235], v[150:153], v[50:53]
	v_add_u32_e32 v142, s38, v200
	v_mfma_f32_16x16x32_bf16 v[38:41], v[224:227], v[158:161], v[38:41]
	v_mfma_f32_16x16x32_bf16 v[34:37], v[232:235], v[158:161], v[34:37]
	v_mfma_f32_16x16x32_bf16 v[22:25], v[224:227], v[166:169], v[22:25]
	v_mfma_f32_16x16x32_bf16 v[18:21], v[232:235], v[166:169], v[18:21]
	v_mfma_f32_16x16x32_bf16 v[6:9], v[224:227], v[174:177], v[6:9]
	v_mfma_f32_16x16x32_bf16 v[2:5], v[232:235], v[174:177], v[2:5]
	s_setprio 0
	s_barrier
	ds_read_b128 v[130:133], v142
	ds_read_b128 v[134:137], v142 offset:1024
	ds_read_b128 v[138:141], v142 offset:2048
	ds_read_b128 v[142:145], v142 offset:3072
	s_mov_b32 m0, s55
	v_lshl_add_u64 v[220:221], s[42:43], 0, v[0:1]
	ds_read_b128 v[146:149], v216 offset:32768
	ds_read_b128 v[150:153], v216 offset:33792
	ds_read_b128 v[154:157], v216 offset:34816
	ds_read_b128 v[158:161], v216 offset:35840
	ds_read_b128 v[162:165], v216 offset:36864
	ds_read_b128 v[166:169], v216 offset:37888
	ds_read_b128 v[170:173], v216 offset:38912
	ds_read_b128 v[174:177], v216 offset:39936
	global_load_lds_dwordx4 v[220:221], off
	v_lshl_add_u64 v[220:221], s[42:43], 0, v[186:187]
	s_mov_b32 m0, s56
	s_nop 0
	global_load_lds_dwordx4 v[220:221], off
	s_waitcnt lgkmcnt(8)
	s_setprio 1
	s_barrier
	s_waitcnt lgkmcnt(0)
	v_mfma_f32_16x16x32_bf16 v[126:129], v[130:133], v[146:149], v[126:129]
	v_mfma_f32_16x16x32_bf16 v[122:125], v[138:141], v[146:149], v[122:125]
	v_mfma_f32_16x16x32_bf16 v[110:113], v[130:133], v[154:157], v[110:113]
	v_mfma_f32_16x16x32_bf16 v[106:109], v[138:141], v[154:157], v[106:109]
	v_mfma_f32_16x16x32_bf16 v[94:97], v[130:133], v[162:165], v[94:97]
	v_mfma_f32_16x16x32_bf16 v[90:93], v[138:141], v[162:165], v[90:93]
	v_mfma_f32_16x16x32_bf16 v[78:81], v[130:133], v[170:173], v[78:81]
	v_mfma_f32_16x16x32_bf16 v[74:77], v[138:141], v[170:173], v[74:77]
	v_mfma_f32_16x16x32_bf16 v[126:129], v[134:137], v[150:153], v[126:129]
	v_mfma_f32_16x16x32_bf16 v[122:125], v[142:145], v[150:153], v[122:125]
	v_mfma_f32_16x16x32_bf16 v[110:113], v[134:137], v[158:161], v[110:113]
	v_mfma_f32_16x16x32_bf16 v[106:109], v[142:145], v[158:161], v[106:109]
	v_mfma_f32_16x16x32_bf16 v[94:97], v[134:137], v[166:169], v[94:97]
	v_mfma_f32_16x16x32_bf16 v[90:93], v[142:145], v[166:169], v[90:93]
	v_mfma_f32_16x16x32_bf16 v[78:81], v[134:137], v[174:177], v[78:81]
	v_mfma_f32_16x16x32_bf16 v[74:77], v[142:145], v[174:177], v[74:77]
	s_setprio 0
	s_barrier
	s_add_i32 s39, 0, 0x1c000
	s_add_i32 s38, s38, s50
	v_add_u32_e32 v183, s39, v200
	v_lshl_add_u64 v[236:237], v[236:237], 0, s[18:19]
	s_mov_b32 m0, s38
	ds_read_b128 v[220:223], v183
	ds_read_b128 v[224:227], v183 offset:1024
	ds_read_b128 v[228:231], v183 offset:2048
	ds_read_b128 v[232:235], v183 offset:3072
	global_load_lds_dwordx4 v[236:237], off
	v_lshl_add_u64 v[236:237], v[238:239], 0, s[18:19]
	s_add_i32 m0, s38, 0x2000
	s_nop 0
	global_load_lds_dwordx4 v[236:237], off
	s_setprio 1
	s_barrier
; #define G8_STAGE(bufoff, gbase, voff) do { _Pragma("unroll") for (int _i = 0; _i < 2; ++_i) \
;         __builtin_amdgcn_global_load_lds((const unsigned*)((const char*)(gbase) + (voff)[_i]), (LAS unsigned*)(lds + (bufoff) + ldsw + _i * 8192), 16, 0, 0); } while (0)
; #define G8_LDA(dst, b, h) do { _Pragma("unroll") for (int m = 0; m < 4; ++m) _Pragma("unroll") for (int k = 0; k < 2; ++k) dst[m][k] = *(const LAS bf16x8*)(lds + G8_SA(b, h) + aoff + m * 2048 + k * 1024); } while (0)
; #define G8_MMA(ai, bj, At, Bt) do { __builtin_amdgcn_s_setprio(1); _Pragma("unroll") for (int m = 0; m < 4; ++m) _Pragma("unroll") for (int n = 0; n < 2; ++n) _Pragma("unroll") for (int k = 0; k < 2; ++k) \
;         acc[ai][bj][m][n] = __builtin_amdgcn_mfma_f32_16x16x32_bf16(Bt[n][k], At[m][k], acc[ai][bj][m][n], 0, 0, 0); __builtin_amdgcn_s_setprio(0); } while (0)
; #define G8_WAIT_V(n) asm volatile("s_waitcnt vmcnt(" #n ")" ::: "memory")
; #define G8_WAIT_L(n) asm volatile("s_waitcnt lgkmcnt(" #n ")" ::: "memory")
; #define G8_BAR __builtin_amdgcn_s_barrier()
; #define G8_SCHED __builtin_amdgcn_sched_barrier(0)
; template <class Epi, class Sched>
; __device__ __forceinline__ void gemm_phase(LAS unsigned char* lds, const int K, const Sched& S, const Epi& E) {
;     ...
;             G8_LDA(At, 1, 1); G8_STAGE(G8_SA(1, 0), a3, oc[0]);
;             G8_BAR; G8_WAIT_L(0); G8_MMA(1, 0, At, B0); G8_BAR; G8_SCHED;
;             G8_STAGE(G8_SB(1, 1), b3 + hstep, voffB);
;             G8_WAIT_V(6); G8_BAR; G8_MMA(1, 1, At, B1); G8_BAR;
;         }
	s_waitcnt lgkmcnt(0)
	v_mfma_f32_16x16x32_bf16 v[118:121], v[220:223], v[146:149], v[118:121]
	v_mfma_f32_16x16x32_bf16 v[114:117], v[228:231], v[146:149], v[114:117]
	v_mfma_f32_16x16x32_bf16 v[102:105], v[220:223], v[154:157], v[102:105]
	v_mfma_f32_16x16x32_bf16 v[98:101], v[228:231], v[154:157], v[98:101]
	v_mfma_f32_16x16x32_bf16 v[86:89], v[220:223], v[162:165], v[86:89]
	v_mfma_f32_16x16x32_bf16 v[82:85], v[228:231], v[162:165], v[82:85]
	v_mfma_f32_16x16x32_bf16 v[70:73], v[220:223], v[170:173], v[70:73]
	v_mfma_f32_16x16x32_bf16 v[66:69], v[228:231], v[170:173], v[66:69]
	v_mfma_f32_16x16x32_bf16 v[118:121], v[224:227], v[150:153], v[118:121]
	s_mov_b32 m0, s57
	v_mfma_f32_16x16x32_bf16 v[114:117], v[232:235], v[150:153], v[114:117]
	v_lshl_add_u64 v[236:237], v[240:241], 0, s[18:19]
	v_mfma_f32_16x16x32_bf16 v[102:105], v[224:227], v[158:161], v[102:105]
	v_mfma_f32_16x16x32_bf16 v[98:101], v[232:235], v[158:161], v[98:101]
	v_mfma_f32_16x16x32_bf16 v[86:89], v[224:227], v[166:169], v[86:89]
	v_mfma_f32_16x16x32_bf16 v[82:85], v[232:235], v[166:169], v[82:85]
	v_mfma_f32_16x16x32_bf16 v[70:73], v[224:227], v[174:177], v[70:73]
	v_mfma_f32_16x16x32_bf16 v[66:69], v[232:235], v[174:177], v[66:69]
	s_setprio 0
	s_barrier
	ds_read_b128 v[146:149], v216 offset:49152
	ds_read_b128 v[150:153], v216 offset:50176
	ds_read_b128 v[154:157], v216 offset:51200
	ds_read_b128 v[158:161], v216 offset:52224
	ds_read_b128 v[162:165], v216 offset:53248
	ds_read_b128 v[166:169], v216 offset:54272
	ds_read_b128 v[170:173], v216 offset:55296
	ds_read_b128 v[174:177], v216 offset:56320
	global_load_lds_dwordx4 v[236:237], off
	v_lshl_add_u64 v[236:237], v[242:243], 0, s[18:19]
	s_mov_b32 m0, s58
	s_nop 0
	global_load_lds_dwordx4 v[236:237], off
	s_setprio 1
	s_barrier
	s_waitcnt lgkmcnt(0)
	v_mfma_f32_16x16x32_bf16 v[62:65], v[130:133], v[146:149], v[62:65]
	v_mfma_f32_16x16x32_bf16 v[58:61], v[138:141], v[146:149], v[58:61]
	v_mfma_f32_16x16x32_bf16 v[46:49], v[130:133], v[154:157], v[46:49]
	v_mfma_f32_16x16x32_bf16 v[42:45], v[138:141], v[154:157], v[42:45]
	v_mfma_f32_16x16x32_bf16 v[30:33], v[130:133], v[162:165], v[30:33]
	v_mfma_f32_16x16x32_bf16 v[26:29], v[138:141], v[162:165], v[26:29]
	v_mfma_f32_16x16x32_bf16 v[14:17], v[130:133], v[170:173], v[14:17]
	v_mfma_f32_16x16x32_bf16 v[10:13], v[138:141], v[170:173], v[10:13]
	v_mfma_f32_16x16x32_bf16 v[62:65], v[134:137], v[150:153], v[62:65]
	v_mfma_f32_16x16x32_bf16 v[58:61], v[142:145], v[150:153], v[58:61]
	v_mfma_f32_16x16x32_bf16 v[46:49], v[134:137], v[158:161], v[46:49]
	v_mfma_f32_16x16x32_bf16 v[42:45], v[142:145], v[158:161], v[42:45]
	v_mfma_f32_16x16x32_bf16 v[30:33], v[134:137], v[166:169], v[30:33]
	v_mfma_f32_16x16x32_bf16 v[26:29], v[142:145], v[166:169], v[26:29]
	v_mfma_f32_16x16x32_bf16 v[14:17], v[134:137], v[174:177], v[14:17]
	v_mfma_f32_16x16x32_bf16 v[10:13], v[142:145], v[174:177], v[10:13]
	s_setprio 0
	s_barrier
	s_add_u32 s36, s36, 0x10080
	s_addc_u32 s37, s37, 0
	s_add_i32 s38, s39, s50
	v_lshl_add_u64 v[130:131], s[36:37], 0, v[178:179]
	s_mov_b32 m0, s38
	s_nop 0
	global_load_lds_dwordx4 v[130:131], off
	v_lshl_add_u64 v[130:131], s[36:37], 0, v[180:181]
	s_add_i32 m0, s38, 0x2000
	s_nop 0
	global_load_lds_dwordx4 v[130:131], off
	s_waitcnt vmcnt(6)
	s_setprio 1
	s_barrier
	v_mfma_f32_16x16x32_bf16 v[54:57], v[220:223], v[146:149], v[54:57]
	v_mfma_f32_16x16x32_bf16 v[50:53], v[228:231], v[146:149], v[50:53]
	v_mfma_f32_16x16x32_bf16 v[38:41], v[220:223], v[154:157], v[38:41]
	v_mfma_f32_16x16x32_bf16 v[34:37], v[228:231], v[154:157], v[34:37]
	v_mfma_f32_16x16x32_bf16 v[22:25], v[220:223], v[162:165], v[22:25]
	v_mfma_f32_16x16x32_bf16 v[18:21], v[228:231], v[162:165], v[18:21]
	v_mfma_f32_16x16x32_bf16 v[6:9], v[220:223], v[170:173], v[6:9]
	v_mfma_f32_16x16x32_bf16 v[2:5], v[228:231], v[170:173], v[2:5]
	v_mfma_f32_16x16x32_bf16 v[54:57], v[224:227], v[150:153], v[54:57]
	v_mfma_f32_16x16x32_bf16 v[50:53], v[232:235], v[150:153], v[50:53]
	v_mfma_f32_16x16x32_bf16 v[38:41], v[224:227], v[158:161], v[38:41]
	v_mfma_f32_16x16x32_bf16 v[34:37], v[232:235], v[158:161], v[34:37]
	v_mfma_f32_16x16x32_bf16 v[22:25], v[224:227], v[166:169], v[22:25]
	v_mfma_f32_16x16x32_bf16 v[18:21], v[232:235], v[166:169], v[18:21]
	v_mfma_f32_16x16x32_bf16 v[6:9], v[224:227], v[174:177], v[6:9]
	v_mfma_f32_16x16x32_bf16 v[2:5], v[232:235], v[174:177], v[2:5]
	s_setprio 0
	s_mov_b64 s[42:43], 0
	s_mov_b64 s[36:37], -1
	s_and_b64 vcc, exec, s[40:41]
	s_barrier
	s_cbranch_vccnz .LBB0_2618
	s_mov_b64 s[38:39], 0x100
	s_branch .LBB0_2614
	s_nop 0
	s_nop 0
	s_nop 0
	s_nop 0
